# speedup vs baseline: 1.0066x; 1.0066x over previous
.Lno_anc:
	s_or_b64 exec, exec, s[8:9]
	v_mov_b32_e32 v7, 0x80
	s_waitcnt vmcnt(0)
	s_sub_u32 s26, 0x1ff, s2
	s_mul_i32 s26, s26, 5
	s_lshr_b32 s26, s26, 6
	s_cmp_eq_u32 s26, 0
	s_cbranch_scc1 .Lhold_done
